# v5 plus MoE gate/up GEMM (ph15/ph17): next tile's expert id and gather-list loads issued a tile ahead (asynchronous), removing two exposed vmcnt(0) round trips per tile
# speedup vs baseline: 1.0176x; 1.0055x over previous
.LBB0_1687:
	v_cndmask_b32_e64 v2, 0, 1, s[62:63]
	v_cmp_ne_u32_e64 s[38:39], 1, v2
	s_andn2_b64 vcc, exec, s[62:63]
	s_mov_b64 s[54:55], s[64:65]
	s_cbranch_vccnz .LBB0_1689
	s_ashr_i32 s53, s52, 31
	s_ashr_i32 s51, s50, 31
	s_lshl_b64 s[54:55], s[52:53], 2
	s_add_u32 s54, s20, s54
	s_addc_u32 s55, s21, s55
	v_mov_b64_e32 v[2:3], s[54:55]
	global_load_dword v1, v[2:3], off sc1
	s_lshl_b64 s[54:55], s[50:51], 18
	s_add_u32 s100, s22, s54
	s_addc_u32 s101, s23, s55
	s_mov_b64 s[54:55], s[64:65]
.LBB0_1689:
	s_andn2_b64 vcc, exec, s[42:43]
	s_cbranch_vccnz .LBB0_1700
	s_lshl_b32 s51, s52, 8
	v_add_u32_e32 v2, s51, v169
	v_add_u32_e32 v4, s51, v205
	s_bitset1_b32 s51, 7
	v_add_u32_e32 v6, s51, v169
	v_add_u32_e32 v8, s51, v205
	v_ashrrev_i32_e32 v3, 31, v2
	v_ashrrev_i32_e32 v5, 31, v4
	v_ashrrev_i32_e32 v7, 31, v6
	v_ashrrev_i32_e32 v9, 31, v8
	v_mov_b32_e32 v181, v167
	v_mov_b32_e32 v183, v167
	s_add_u32 s51, s64, 0x100
	v_mov_b32_e32 v34, 0
	v_lshl_add_u64 v[184:185], v[2:3], 2, s[30:31]
	v_lshl_add_u64 v[186:187], v[4:5], 2, s[30:31]
	v_lshl_add_u64 v[188:189], v[6:7], 2, s[30:31]
	v_lshl_add_u64 v[190:191], v[8:9], 2, s[30:31]
	s_addc_u32 s53, s65, 0
	s_and_b64 vcc, exec, s[62:63]
	s_cbranch_vccz .Lnolist_15
	global_load_dword v184, v[184:185], off
	global_load_dword v186, v[186:187], off
	global_load_dword v188, v[188:189], off
	global_load_dword v190, v[190:191], off
.Lnolist_15:
	v_lshl_add_u64 v[192:193], s[40:41], 0, v[182:183]
	v_lshl_add_u64 v[194:195], s[40:41], 0, v[180:181]
	s_mov_b32 s91, 0
	s_mov_b64 s[70:71], 0
	v_mov_b32_e32 v35, v34
	v_mov_b32_e32 v36, v34
	v_mov_b32_e32 v37, v34
	v_mov_b32_e32 v42, v34
	v_mov_b32_e32 v43, v34
	v_mov_b32_e32 v44, v34
	v_mov_b32_e32 v45, v34
	v_mov_b32_e32 v50, v34
	v_mov_b32_e32 v51, v34
	v_mov_b32_e32 v52, v34
	v_mov_b32_e32 v53, v34
	v_mov_b32_e32 v58, v34
	v_mov_b32_e32 v59, v34
	v_mov_b32_e32 v60, v34
	v_mov_b32_e32 v61, v34
	v_mov_b32_e32 v66, v34
	v_mov_b32_e32 v67, v34
	v_mov_b32_e32 v68, v34
	v_mov_b32_e32 v69, v34
	v_mov_b32_e32 v74, v34
	v_mov_b32_e32 v75, v34
	v_mov_b32_e32 v76, v34
	v_mov_b32_e32 v77, v34
	v_mov_b32_e32 v82, v34
	v_mov_b32_e32 v83, v34
	v_mov_b32_e32 v84, v34
	v_mov_b32_e32 v85, v34
	v_mov_b32_e32 v90, v34
	v_mov_b32_e32 v91, v34
	v_mov_b32_e32 v92, v34
	v_mov_b32_e32 v93, v34
	v_mov_b32_e32 v38, v34
	v_mov_b32_e32 v39, v34
	v_mov_b32_e32 v40, v34
	v_mov_b32_e32 v41, v34
	v_mov_b32_e32 v46, v34
	v_mov_b32_e32 v47, v34
	v_mov_b32_e32 v48, v34
	v_mov_b32_e32 v49, v34
	v_mov_b32_e32 v54, v34
	v_mov_b32_e32 v55, v34
	v_mov_b32_e32 v56, v34
	v_mov_b32_e32 v57, v34
	v_mov_b32_e32 v62, v34
	v_mov_b32_e32 v63, v34
	v_mov_b32_e32 v64, v34
	v_mov_b32_e32 v65, v34
	v_mov_b32_e32 v70, v34
	v_mov_b32_e32 v71, v34
	v_mov_b32_e32 v72, v34
	v_mov_b32_e32 v73, v34
	v_mov_b32_e32 v78, v34
	v_mov_b32_e32 v79, v34
	v_mov_b32_e32 v80, v34
	v_mov_b32_e32 v81, v34
	v_mov_b32_e32 v86, v34
	v_mov_b32_e32 v87, v34
	v_mov_b32_e32 v88, v34
	v_mov_b32_e32 v89, v34
	v_mov_b32_e32 v94, v34
	v_mov_b32_e32 v95, v34
	v_mov_b32_e32 v96, v34
	v_mov_b32_e32 v97, v34
	v_mov_b32_e32 v98, v34
	v_mov_b32_e32 v99, v34
	v_mov_b32_e32 v100, v34
	v_mov_b32_e32 v101, v34
	v_mov_b32_e32 v106, v34
	v_mov_b32_e32 v107, v34
	v_mov_b32_e32 v108, v34
	v_mov_b32_e32 v109, v34
	v_mov_b32_e32 v114, v34
	v_mov_b32_e32 v115, v34
	v_mov_b32_e32 v116, v34
	v_mov_b32_e32 v117, v34
	v_mov_b32_e32 v122, v34
	v_mov_b32_e32 v123, v34
	v_mov_b32_e32 v124, v34
	v_mov_b32_e32 v125, v34
	v_mov_b32_e32 v130, v34
	v_mov_b32_e32 v131, v34
	v_mov_b32_e32 v132, v34
	v_mov_b32_e32 v133, v34
	v_mov_b32_e32 v138, v34
	v_mov_b32_e32 v139, v34
	v_mov_b32_e32 v140, v34
	v_mov_b32_e32 v141, v34
	v_mov_b32_e32 v146, v34
	v_mov_b32_e32 v147, v34
	v_mov_b32_e32 v148, v34
	v_mov_b32_e32 v149, v34
	v_mov_b32_e32 v158, v34
	v_mov_b32_e32 v159, v34
	v_mov_b32_e32 v160, v34
	v_mov_b32_e32 v161, v34
	v_mov_b32_e32 v102, v34
	v_mov_b32_e32 v103, v34
	v_mov_b32_e32 v104, v34
	v_mov_b32_e32 v105, v34
	v_mov_b32_e32 v110, v34
	v_mov_b32_e32 v111, v34
	v_mov_b32_e32 v112, v34
	v_mov_b32_e32 v113, v34
	v_mov_b32_e32 v118, v34
	v_mov_b32_e32 v119, v34
	v_mov_b32_e32 v120, v34
	v_mov_b32_e32 v121, v34
	v_mov_b32_e32 v126, v34
	v_mov_b32_e32 v127, v34
	v_mov_b32_e32 v128, v34
	v_mov_b32_e32 v129, v34
	v_mov_b32_e32 v134, v34
	v_mov_b32_e32 v135, v34
	v_mov_b32_e32 v136, v34
	v_mov_b32_e32 v137, v34
	v_mov_b32_e32 v142, v34
	v_mov_b32_e32 v143, v34
	v_mov_b32_e32 v144, v34
	v_mov_b32_e32 v145, v34
	v_mov_b32_e32 v150, v34
	v_mov_b32_e32 v151, v34
	v_mov_b32_e32 v152, v34
	v_mov_b32_e32 v153, v34
	v_mov_b32_e32 v154, v34
	v_mov_b32_e32 v155, v34
	v_mov_b32_e32 v156, v34
	v_mov_b32_e32 v157, v34
.LBB0_1691:
	s_cmp_eq_u32 s88, s91
	s_cselect_b64 s[68:69], -1, 0
	s_and_b64 s[64:65], s[62:63], s[68:69]
	s_andn2_b64 vcc, exec, s[64:65]
	s_cbranch_vccnz .LBB0_1693
	v_readfirstlane_b32 s54, v1
	v_lshlrev_b32_e32 v2, 9, v184
	v_lshlrev_b32_e32 v3, 9, v186
	v_lshlrev_b32_e32 v4, 9, v188
	v_lshlrev_b32_e32 v5, 9, v190
	s_mul_hi_u32 s55, s54, 0x700000
	s_mul_i32 s54, s54, 0x700000
	s_add_u32 s54, s100, s54
	s_addc_u32 s55, s101, s55
	v_and_b32_e32 v2, 0x1fffe00, v2
	v_and_b32_e32 v3, 0x1fffe00, v3
	v_and_b32_e32 v4, 0x1fffe00, v4
	v_and_b32_e32 v5, 0x1fffe00, v5
	v_add_lshl_u32 v166, v2, v204, 1
	v_add_lshl_u32 v178, v3, v206, 1
	v_add_lshl_u32 v180, v4, v204, 1
	v_add_lshl_u32 v182, v5, v206, 1

.LBB0_1832:
	s_andn2_b64 vcc, exec, s[50:51]
	s_mov_b64 s[52:53], s[60:61]
	s_cbranch_vccnz .LBB0_1834
	s_ashr_i32 s49, s48, 31
	s_ashr_i32 s47, s46, 31
	s_lshl_b64 s[52:53], s[48:49], 2
	s_add_u32 s52, s23, s52
	s_addc_u32 s53, s70, s53
	v_mov_b64_e32 v[2:3], s[52:53]
	global_load_dword v1, v[2:3], off sc1
	s_lshl_b64 s[52:53], s[46:47], 18
	s_add_u32 s100, s20, s52
	s_addc_u32 s101, s21, s53
	s_mov_b64 s[52:53], s[60:61]
.LBB0_1834:
	s_andn2_b64 vcc, exec, s[40:41]
	s_cbranch_vccnz .LBB0_1840
	s_lshl_b32 s47, s48, 8
	v_add_u32_e32 v2, s47, v169
	v_add_u32_e32 v4, s47, v205
	s_bitset1_b32 s47, 7
	v_add_u32_e32 v6, s47, v169
	v_add_u32_e32 v8, s47, v205
	v_ashrrev_i32_e32 v3, 31, v2
	v_ashrrev_i32_e32 v5, 31, v4
	v_ashrrev_i32_e32 v7, 31, v6
	v_ashrrev_i32_e32 v9, 31, v8
	v_mov_b32_e32 v181, v167
	v_mov_b32_e32 v183, v167
	s_add_u32 s47, s60, 0x100
	v_mov_b32_e32 v34, 0
	v_lshl_add_u64 v[184:185], v[2:3], 2, s[28:29]
	v_lshl_add_u64 v[186:187], v[4:5], 2, s[28:29]
	v_lshl_add_u64 v[188:189], v[6:7], 2, s[28:29]
	v_lshl_add_u64 v[190:191], v[8:9], 2, s[28:29]
	s_addc_u32 s49, s61, 0
	s_and_b64 vcc, exec, s[50:51]
	s_cbranch_vccz .Lnolist_17
	global_load_dword v184, v[184:185], off
	global_load_dword v186, v[186:187], off
	global_load_dword v188, v[188:189], off
	global_load_dword v190, v[190:191], off
.Lnolist_17:
	v_lshl_add_u64 v[192:193], s[38:39], 0, v[182:183]
	v_lshl_add_u64 v[194:195], s[38:39], 0, v[180:181]
	s_mov_b32 s55, 0
	s_mov_b64 s[64:65], 0
	v_mov_b32_e32 v35, v34
	v_mov_b32_e32 v36, v34
	v_mov_b32_e32 v37, v34
	v_mov_b32_e32 v42, v34
	v_mov_b32_e32 v43, v34
	v_mov_b32_e32 v44, v34
	v_mov_b32_e32 v45, v34
	v_mov_b32_e32 v50, v34
	v_mov_b32_e32 v51, v34
	v_mov_b32_e32 v52, v34
	v_mov_b32_e32 v53, v34
	v_mov_b32_e32 v58, v34
	v_mov_b32_e32 v59, v34
	v_mov_b32_e32 v60, v34
	v_mov_b32_e32 v61, v34
	v_mov_b32_e32 v66, v34
	v_mov_b32_e32 v67, v34
	v_mov_b32_e32 v68, v34
	v_mov_b32_e32 v69, v34
	v_mov_b32_e32 v74, v34
	v_mov_b32_e32 v75, v34
	v_mov_b32_e32 v76, v34
	v_mov_b32_e32 v77, v34
	v_mov_b32_e32 v82, v34
	v_mov_b32_e32 v83, v34
	v_mov_b32_e32 v84, v34
	v_mov_b32_e32 v85, v34
	v_mov_b32_e32 v90, v34
	v_mov_b32_e32 v91, v34
	v_mov_b32_e32 v92, v34
	v_mov_b32_e32 v93, v34
	v_mov_b32_e32 v38, v34
	v_mov_b32_e32 v39, v34
	v_mov_b32_e32 v40, v34
	v_mov_b32_e32 v41, v34
	v_mov_b32_e32 v46, v34
	v_mov_b32_e32 v47, v34
	v_mov_b32_e32 v48, v34
	v_mov_b32_e32 v49, v34
	v_mov_b32_e32 v54, v34
	v_mov_b32_e32 v55, v34
	v_mov_b32_e32 v56, v34
	v_mov_b32_e32 v57, v34
	v_mov_b32_e32 v62, v34
	v_mov_b32_e32 v63, v34
	v_mov_b32_e32 v64, v34
	v_mov_b32_e32 v65, v34
	v_mov_b32_e32 v70, v34
	v_mov_b32_e32 v71, v34
	v_mov_b32_e32 v72, v34
	v_mov_b32_e32 v73, v34
	v_mov_b32_e32 v78, v34
	v_mov_b32_e32 v79, v34
	v_mov_b32_e32 v80, v34
	v_mov_b32_e32 v81, v34
	v_mov_b32_e32 v86, v34
	v_mov_b32_e32 v87, v34
	v_mov_b32_e32 v88, v34
	v_mov_b32_e32 v89, v34
	v_mov_b32_e32 v94, v34
	v_mov_b32_e32 v95, v34
	v_mov_b32_e32 v96, v34
	v_mov_b32_e32 v97, v34
	v_mov_b32_e32 v98, v34
	v_mov_b32_e32 v99, v34
	v_mov_b32_e32 v100, v34
	v_mov_b32_e32 v101, v34
	v_mov_b32_e32 v106, v34
	v_mov_b32_e32 v107, v34
	v_mov_b32_e32 v108, v34
	v_mov_b32_e32 v109, v34
	v_mov_b32_e32 v114, v34
	v_mov_b32_e32 v115, v34
	v_mov_b32_e32 v116, v34
	v_mov_b32_e32 v117, v34
	v_mov_b32_e32 v122, v34
	v_mov_b32_e32 v123, v34
	v_mov_b32_e32 v124, v34
	v_mov_b32_e32 v125, v34
	v_mov_b32_e32 v130, v34
	v_mov_b32_e32 v131, v34
	v_mov_b32_e32 v132, v34
	v_mov_b32_e32 v133, v34
	v_mov_b32_e32 v138, v34
	v_mov_b32_e32 v139, v34
	v_mov_b32_e32 v140, v34
	v_mov_b32_e32 v141, v34
	v_mov_b32_e32 v146, v34
	v_mov_b32_e32 v147, v34
	v_mov_b32_e32 v148, v34
	v_mov_b32_e32 v149, v34
	v_mov_b32_e32 v158, v34
	v_mov_b32_e32 v159, v34
	v_mov_b32_e32 v160, v34
	v_mov_b32_e32 v161, v34
	v_mov_b32_e32 v102, v34
	v_mov_b32_e32 v103, v34
	v_mov_b32_e32 v104, v34
	v_mov_b32_e32 v105, v34
	v_mov_b32_e32 v110, v34
	v_mov_b32_e32 v111, v34
	v_mov_b32_e32 v112, v34
	v_mov_b32_e32 v113, v34
	v_mov_b32_e32 v118, v34
	v_mov_b32_e32 v119, v34
	v_mov_b32_e32 v120, v34
	v_mov_b32_e32 v121, v34
	v_mov_b32_e32 v126, v34
	v_mov_b32_e32 v127, v34
	v_mov_b32_e32 v128, v34
	v_mov_b32_e32 v129, v34
	v_mov_b32_e32 v134, v34
	v_mov_b32_e32 v135, v34
	v_mov_b32_e32 v136, v34
	v_mov_b32_e32 v137, v34
	v_mov_b32_e32 v142, v34
	v_mov_b32_e32 v143, v34
	v_mov_b32_e32 v144, v34
	v_mov_b32_e32 v145, v34
	v_mov_b32_e32 v150, v34
	v_mov_b32_e32 v151, v34
	v_mov_b32_e32 v152, v34
	v_mov_b32_e32 v153, v34
	v_mov_b32_e32 v154, v34
	v_mov_b32_e32 v155, v34
	v_mov_b32_e32 v156, v34
	v_mov_b32_e32 v157, v34
.LBB0_1836:
	s_cmp_eq_u32 s77, s55
	s_cselect_b64 s[62:63], -1, 0
	s_and_b64 s[60:61], s[50:51], s[62:63]
	s_andn2_b64 vcc, exec, s[60:61]
	s_cbranch_vccnz .LBB0_1838
	v_readfirstlane_b32 s52, v1
	v_lshlrev_b32_e32 v2, 9, v184
	v_lshlrev_b32_e32 v3, 9, v186
	v_lshlrev_b32_e32 v4, 9, v188
	v_lshlrev_b32_e32 v5, 9, v190
	s_mul_hi_u32 s53, s52, 0x700000
	s_mul_i32 s52, s52, 0x700000
	s_add_u32 s52, s100, s52
	s_addc_u32 s53, s101, s53
	v_and_b32_e32 v2, 0x1fffe00, v2
	v_and_b32_e32 v3, 0x1fffe00, v3
	v_and_b32_e32 v4, 0x1fffe00, v4
	v_and_b32_e32 v5, 0x1fffe00, v5
	v_add_lshl_u32 v166, v2, v204, 1
	v_add_lshl_u32 v178, v3, v206, 1
	v_add_lshl_u32 v180, v4, v204, 1
	v_add_lshl_u32 v182, v5, v206, 1

	.amdhsa_kernel _Z9trunk_fwd4Args
		.amdhsa_group_segment_fixed_size 0
		.amdhsa_private_segment_fixed_size 0
		.amdhsa_kernarg_size 472
		.amdhsa_user_sgpr_count 2
		.amdhsa_user_sgpr_dispatch_ptr 0
		.amdhsa_user_sgpr_queue_ptr 0
		.amdhsa_user_sgpr_kernarg_segment_ptr 1
		.amdhsa_user_sgpr_dispatch_id 0
		.amdhsa_user_sgpr_kernarg_preload_length 0
		.amdhsa_user_sgpr_kernarg_preload_offset 0
		.amdhsa_user_sgpr_private_segment_size 0
		.amdhsa_uses_dynamic_stack 0
		.amdhsa_enable_private_segment 0
		.amdhsa_system_sgpr_workgroup_id_x 1
		.amdhsa_system_sgpr_workgroup_id_y 0
		.amdhsa_system_sgpr_workgroup_id_z 0
		.amdhsa_system_sgpr_workgroup_info 0
		.amdhsa_system_vgpr_workitem_id 0
		.amdhsa_next_free_vgpr 256
		.amdhsa_next_free_sgpr 102
		.amdhsa_accum_offset 256
		.amdhsa_reserve_vcc 1
		.amdhsa_float_round_mode_32 0
		.amdhsa_float_round_mode_16_64 0
		.amdhsa_float_denorm_mode_32 3
		.amdhsa_float_denorm_mode_16_64 3
		.amdhsa_dx10_clamp 1
		.amdhsa_ieee_mode 1
		.amdhsa_fp16_overflow 0
		.amdhsa_tg_split 0
		.amdhsa_exception_fp_ieee_invalid_op 0
		.amdhsa_exception_fp_denorm_src 0
		.amdhsa_exception_fp_ieee_div_zero 0
		.amdhsa_exception_fp_ieee_overflow 0
		.amdhsa_exception_fp_ieee_underflow 0
		.amdhsa_exception_fp_ieee_inexact 0
		.amdhsa_exception_int_div_zero 0
	.end_amdhsa_kernel

amdhsa.kernels:
  - .agpr_count:     0
    .args:
      - .offset:         0
        .size:           216
        .value_kind:     by_value
      - .offset:         216
        .size:           4
        .value_kind:     hidden_block_count_x
      - .offset:         220
        .size:           4
        .value_kind:     hidden_block_count_y
      - .offset:         224
        .size:           4
        .value_kind:     hidden_block_count_z
      - .offset:         228
        .size:           2
        .value_kind:     hidden_group_size_x
      - .offset:         230
        .size:           2
        .value_kind:     hidden_group_size_y
      - .offset:         232
        .size:           2
        .value_kind:     hidden_group_size_z
      - .offset:         234
        .size:           2
        .value_kind:     hidden_remainder_x
      - .offset:         236
        .size:           2
        .value_kind:     hidden_remainder_y
      - .offset:         238
        .size:           2
        .value_kind:     hidden_remainder_z
      - .offset:         256
        .size:           8
        .value_kind:     hidden_global_offset_x
      - .offset:         264
        .size:           8
        .value_kind:     hidden_global_offset_y
      - .offset:         272
        .size:           8
        .value_kind:     hidden_global_offset_z
      - .offset:         280
        .size:           2
        .value_kind:     hidden_grid_dims
      - .offset:         336
        .size:           4
        .value_kind:     hidden_dynamic_lds_size
    .group_segment_fixed_size: 0
    .kernarg_segment_align: 8
    .kernarg_segment_size: 472
    .language:       OpenCL C
    .language_version:
      - 2
      - 0
    .max_flat_workgroup_size: 512
    .name:           _Z9trunk_fwd4Args
    .private_segment_fixed_size: 0
    .sgpr_count:     108
    .sgpr_spill_count: 87
    .symbol:         _Z9trunk_fwd4Args.kd
    .uniform_work_group_size: 1
    .uses_dynamic_stack: false
    .vgpr_count:     256
    .vgpr_spill_count: 0
    .wavefront_size: 64
